# speedup vs baseline: 1.0132x; 1.0036x over previous
.LBB1_2:
	s_mul_i32 s41, s34, 0x30000
	s_mul_hi_i32 s40, s34, 0x30000
	s_add_u32 s11, s6, s41
	s_addc_u32 s35, s7, s40
	s_mov_b32 s10, s2
	s_add_u32 s2, s11, 0x6000
	s_addc_u32 s3, s35, 0
	s_mul_i32 s43, s13, 0x30000
	s_mul_hi_i32 s42, s13, 0x30000
	s_add_u32 s44, s4, s43
	s_addc_u32 s45, s5, s42
	s_add_u32 s38, s11, 0x8000
	s_addc_u32 s39, s35, 0
	s_add_u32 s46, s44, 0x5000
	s_addc_u32 s47, s45, 0
	s_and_b64 s[36:37], s[0:1], exec
	s_cselect_b32 s37, s39, s47
	s_cselect_b32 s36, s38, s46
	s_add_u32 s38, s44, 0x7000
	s_addc_u32 s39, s45, 0
	s_add_u32 s2, s11, 0x9000
	s_addc_u32 s3, s35, 0
	s_add_u32 s11, s11, 0xb000
	s_addc_u32 s35, s35, 0
	s_add_u32 s38, s44, 0x8000
	s_addc_u32 s39, s45, 0
	s_and_b64 s[36:37], s[0:1], exec
	s_cselect_b32 s37, s35, s39
	s_cselect_b32 s36, s11, s38
	s_add_u32 s38, s44, 0xa000
	s_addc_u32 s39, s45, 0
	s_add_u32 s11, s21, s43
	s_addc_u32 s35, s22, s42
	s_add_u32 s2, s23, s41
	s_addc_u32 s3, s24, s40
	s_cmp_eq_u32 s74, 1
	s_cselect_b32 s72, s11, s2
	s_cselect_b32 s73, s35, s3
	s_add_u32 s72, s72, s75
	s_addc_u32 s73, s73, 0
	s_mov_b32 s36, -2
	s_cmp_eq_u32 s66, 0
	s_cselect_b64 vcc, exec, 0
	s_waitcnt lgkmcnt(0)
.Lgemm_peel:
	ds_read_b128 v[188:191], v1 offset:24576
	ds_read_b64 v[192:193], v172 offset:24640
	ds_read_b128 v[194:197], v1 offset:26112
	ds_read_b64 v[198:199], v172 offset:26176
	ds_read_b128 v[200:203], v170 offset:36864
	ds_read_b64 v[204:205], v173 offset:36928
	ds_read_b128 v[206:209], v170 offset:38400
	ds_read_b64 v[210:211], v173 offset:38464
	ds_read_b128 v[212:215], v170 offset:39936
	ds_read_b64 v[216:217], v173 offset:40000
	ds_read_b128 v[218:221], v170 offset:41472
	ds_read_b64 v[222:223], v173 offset:41536
	v_mfma_scale_f32_16x16x128_f8f6f4 v[164:167], v[2:7], v[20:25], 0, v187, v187 op_sel_hi:[0,0,0] cbsz:2 blgp:2
	v_mfma_scale_f32_16x16x128_f8f6f4 v[160:163], v[8:13], v[20:25], 0, v187, v187 op_sel_hi:[0,0,0] cbsz:2 blgp:2
	v_mfma_scale_f32_16x16x128_f8f6f4 v[156:159], v[14:19], v[20:25], 0, v187, v187 op_sel_hi:[0,0,0] cbsz:2 blgp:2
	v_mfma_scale_f32_16x16x128_f8f6f4 v[152:155], v[26:31], v[20:25], 0, v187, v187 op_sel_hi:[0,0,0] cbsz:2 blgp:2
	v_mfma_scale_f32_16x16x128_f8f6f4 v[148:151], v[2:7], v[32:37], 0, v187, v187 op_sel_hi:[0,0,0] cbsz:2 blgp:2
	v_mfma_scale_f32_16x16x128_f8f6f4 v[140:143], v[8:13], v[32:37], 0, v187, v187 op_sel_hi:[0,0,0] cbsz:2 blgp:2
	v_mfma_scale_f32_16x16x128_f8f6f4 v[132:135], v[14:19], v[32:37], 0, v187, v187 op_sel_hi:[0,0,0] cbsz:2 blgp:2
	v_mfma_scale_f32_16x16x128_f8f6f4 v[124:127], v[26:31], v[32:37], 0, v187, v187 op_sel_hi:[0,0,0] cbsz:2 blgp:2
	s_cbranch_vccz .Lpst0_other
	s_add_u32 s38, s72, 0xffffa000
	s_addc_u32 s39, s73, -1
	s_waitcnt vmcnt(0)
	s_barrier
	s_mov_b32 m0, s76
	s_nop 0
	global_load_lds_dwordx4 v228, s[38:39] offset:-3072
	global_load_lds_dwordx4 v228, s[38:39] offset:-2048
	global_load_lds_dwordx4 v228, s[38:39] offset:-1024
	global_load_lds_dwordx4 v228, s[38:39]
	global_load_lds_dwordx4 v228, s[38:39] offset:1024
	global_load_lds_dwordx4 v228, s[38:39] offset:2048
	s_branch .Lpst0_join

.Lpst0_join:
	s_waitcnt lgkmcnt(0)
	v_mfma_scale_f32_16x16x128_f8f6f4 v[112:115], v[2:7], v[188:193], 0, v187, v187 op_sel_hi:[0,0,0] cbsz:2 blgp:2
	v_mfma_scale_f32_16x16x128_f8f6f4 v[100:103], v[8:13], v[188:193], 0, v187, v187 op_sel_hi:[0,0,0] cbsz:2 blgp:2
	v_mfma_scale_f32_16x16x128_f8f6f4 v[92:95], v[14:19], v[188:193], 0, v187, v187 op_sel_hi:[0,0,0] cbsz:2 blgp:2
	v_mfma_scale_f32_16x16x128_f8f6f4 v[88:91], v[26:31], v[188:193], 0, v187, v187 op_sel_hi:[0,0,0] cbsz:2 blgp:2
	v_mfma_scale_f32_16x16x128_f8f6f4 v[84:87], v[2:7], v[194:199], 0, v187, v187 op_sel_hi:[0,0,0] cbsz:2 blgp:2
	v_mfma_scale_f32_16x16x128_f8f6f4 v[76:79], v[8:13], v[194:199], 0, v187, v187 op_sel_hi:[0,0,0] cbsz:2 blgp:2
	v_mfma_scale_f32_16x16x128_f8f6f4 v[68:71], v[14:19], v[194:199], 0, v187, v187 op_sel_hi:[0,0,0] cbsz:2 blgp:2
	v_mfma_scale_f32_16x16x128_f8f6f4 v[60:63], v[26:31], v[194:199], 0, v187, v187 op_sel_hi:[0,0,0] cbsz:2 blgp:2
	ds_read_b128 v[2:5], v170 offset:61440
	ds_read_b64 v[6:7], v173 offset:61504
	ds_read_b128 v[8:11], v170 offset:62976
	ds_read_b64 v[12:13], v173 offset:63040
	ds_read_b128 v[14:17], v170 offset:64512
	ds_read_b64 v[18:19], v173 offset:64576
	ds_read_b128 v[26:29], v171 offset:53760
	ds_read_b64 v[30:31], v174 offset:53760
	v_mfma_scale_f32_16x16x128_f8f6f4 v[144:147], v[200:205], v[20:25], 0, v187, v187 op_sel_hi:[0,0,0] cbsz:2 blgp:2
	v_mfma_scale_f32_16x16x128_f8f6f4 v[136:139], v[206:211], v[20:25], 0, v187, v187 op_sel_hi:[0,0,0] cbsz:2 blgp:2
	v_mfma_scale_f32_16x16x128_f8f6f4 v[128:131], v[212:217], v[20:25], 0, v187, v187 op_sel_hi:[0,0,0] cbsz:2 blgp:2
	v_mfma_scale_f32_16x16x128_f8f6f4 v[120:123], v[218:223], v[20:25], 0, v187, v187 op_sel_hi:[0,0,0] cbsz:2 blgp:2
	v_mfma_scale_f32_16x16x128_f8f6f4 v[116:119], v[200:205], v[32:37], 0, v187, v187 op_sel_hi:[0,0,0] cbsz:2 blgp:2
	v_mfma_scale_f32_16x16x128_f8f6f4 v[108:111], v[206:211], v[32:37], 0, v187, v187 op_sel_hi:[0,0,0] cbsz:2 blgp:2
	v_mfma_scale_f32_16x16x128_f8f6f4 v[104:107], v[212:217], v[32:37], 0, v187, v187 op_sel_hi:[0,0,0] cbsz:2 blgp:2
	v_mfma_scale_f32_16x16x128_f8f6f4 v[96:99], v[218:223], v[32:37], 0, v187, v187 op_sel_hi:[0,0,0] cbsz:2 blgp:2
	ds_read_b128 v[20:23], v1 offset:49152
	ds_read_b64 v[24:25], v172 offset:49216
	ds_read_b128 v[32:35], v1 offset:50688
	ds_read_b64 v[36:37], v172 offset:50752
	s_cbranch_vccnz .Lpst1_other
	s_add_u32 s38, s72, 0xffffd000
	s_addc_u32 s39, s73, -1
	s_waitcnt vmcnt(0)
	s_barrier
	s_mov_b32 m0, s76
	s_nop 0
	global_load_lds_dwordx4 v228, s[38:39] offset:-3072
	global_load_lds_dwordx4 v228, s[38:39] offset:-2048
	global_load_lds_dwordx4 v228, s[38:39] offset:-1024
	global_load_lds_dwordx4 v228, s[38:39]
	global_load_lds_dwordx4 v228, s[38:39] offset:1024
	global_load_lds_dwordx4 v228, s[38:39] offset:2048
	s_branch .Lpst1_join

.Lpst1_join:
	v_mfma_scale_f32_16x16x128_f8f6f4 v[80:83], v[200:205], v[188:193], 0, v187, v187 op_sel_hi:[0,0,0] cbsz:2 blgp:2
	v_mfma_scale_f32_16x16x128_f8f6f4 v[72:75], v[206:211], v[188:193], 0, v187, v187 op_sel_hi:[0,0,0] cbsz:2 blgp:2
	v_mfma_scale_f32_16x16x128_f8f6f4 v[64:67], v[212:217], v[188:193], 0, v187, v187 op_sel_hi:[0,0,0] cbsz:2 blgp:2
	v_mfma_scale_f32_16x16x128_f8f6f4 v[56:59], v[218:223], v[188:193], 0, v187, v187 op_sel_hi:[0,0,0] cbsz:2 blgp:2
	v_mfma_scale_f32_16x16x128_f8f6f4 v[52:55], v[200:205], v[194:199], 0, v187, v187 op_sel_hi:[0,0,0] cbsz:2 blgp:2
	v_mfma_scale_f32_16x16x128_f8f6f4 v[224:227], v[206:211], v[194:199], 0, v187, v187 op_sel_hi:[0,0,0] cbsz:2 blgp:2
	v_mfma_scale_f32_16x16x128_f8f6f4 v[212:215], v[212:217], v[194:199], 0, v187, v187 op_sel_hi:[0,0,0] cbsz:2 blgp:2
	v_mfma_scale_f32_16x16x128_f8f6f4 v[216:219], v[218:223], v[194:199], 0, v187, v187 op_sel_hi:[0,0,0] cbsz:2 blgp:2
	s_waitcnt lgkmcnt(0)
	s_nop 0
	ds_read_b128 v[40:43], v175
	ds_read_b64 v[44:45], v176
	ds_read_b128 v[188:191], v179
	ds_read_b64 v[192:193], v180
	ds_read_b128 v[46:49], v177
	ds_read_b64 v[50:51], v178
	ds_read_b128 v[194:197], v181
	ds_read_b64 v[198:199], v182
	ds_read_b128 v[200:203], v183
	ds_read_b64 v[204:205], v184
	ds_read_b128 v[206:209], v185
	ds_read_b64 v[210:211], v186
	v_mfma_scale_f32_16x16x128_f8f6f4 v[164:167], v[2:7], v[20:25], v[164:167], v187, v187 op_sel_hi:[0,0,0] cbsz:2 blgp:2
	v_mfma_scale_f32_16x16x128_f8f6f4 v[160:163], v[8:13], v[20:25], v[160:163], v187, v187 op_sel_hi:[0,0,0] cbsz:2 blgp:2
	v_mfma_scale_f32_16x16x128_f8f6f4 v[156:159], v[14:19], v[20:25], v[156:159], v187, v187 op_sel_hi:[0,0,0] cbsz:2 blgp:2
	v_mfma_scale_f32_16x16x128_f8f6f4 v[152:155], v[26:31], v[20:25], v[152:155], v187, v187 op_sel_hi:[0,0,0] cbsz:2 blgp:2
	v_mfma_scale_f32_16x16x128_f8f6f4 v[148:151], v[2:7], v[32:37], v[148:151], v187, v187 op_sel_hi:[0,0,0] cbsz:2 blgp:2
	v_mfma_scale_f32_16x16x128_f8f6f4 v[140:143], v[8:13], v[32:37], v[140:143], v187, v187 op_sel_hi:[0,0,0] cbsz:2 blgp:2
	v_mfma_scale_f32_16x16x128_f8f6f4 v[132:135], v[14:19], v[32:37], v[132:135], v187, v187 op_sel_hi:[0,0,0] cbsz:2 blgp:2
	v_mfma_scale_f32_16x16x128_f8f6f4 v[124:127], v[26:31], v[32:37], v[124:127], v187, v187 op_sel_hi:[0,0,0] cbsz:2 blgp:2
	s_cbranch_vccz .Lpst2_other
	s_mov_b64 s[38:39], s[72:73]
	s_waitcnt vmcnt(0)
	s_barrier
	s_mov_b32 m0, s77
	s_nop 0
	global_load_lds_dwordx4 v228, s[38:39] offset:-3072
	global_load_lds_dwordx4 v228, s[38:39] offset:-2048
	global_load_lds_dwordx4 v228, s[38:39] offset:-1024
	global_load_lds_dwordx4 v228, s[38:39]
	global_load_lds_dwordx4 v228, s[38:39] offset:1024
	global_load_lds_dwordx4 v228, s[38:39] offset:2048
	s_branch .Lpst2_join

.Lpst2_join:
	s_waitcnt lgkmcnt(0)
	v_mfma_scale_f32_16x16x128_f8f6f4 v[112:115], v[2:7], v[40:45], v[112:115], v187, v187 op_sel_hi:[0,0,0] cbsz:2 blgp:2
	v_mfma_scale_f32_16x16x128_f8f6f4 v[100:103], v[8:13], v[40:45], v[100:103], v187, v187 op_sel_hi:[0,0,0] cbsz:2 blgp:2
	v_mfma_scale_f32_16x16x128_f8f6f4 v[92:95], v[14:19], v[40:45], v[92:95], v187, v187 op_sel_hi:[0,0,0] cbsz:2 blgp:2
	v_mfma_scale_f32_16x16x128_f8f6f4 v[88:91], v[26:31], v[40:45], v[88:91], v187, v187 op_sel_hi:[0,0,0] cbsz:2 blgp:2
	v_mfma_scale_f32_16x16x128_f8f6f4 v[84:87], v[2:7], v[188:193], v[84:87], v187, v187 op_sel_hi:[0,0,0] cbsz:2 blgp:2
	v_mfma_scale_f32_16x16x128_f8f6f4 v[76:79], v[8:13], v[188:193], v[76:79], v187, v187 op_sel_hi:[0,0,0] cbsz:2 blgp:2
	v_mfma_scale_f32_16x16x128_f8f6f4 v[68:71], v[14:19], v[188:193], v[68:71], v187, v187 op_sel_hi:[0,0,0] cbsz:2 blgp:2
	v_mfma_scale_f32_16x16x128_f8f6f4 v[60:63], v[26:31], v[188:193], v[60:63], v187, v187 op_sel_hi:[0,0,0] cbsz:2 blgp:2
	ds_read_b128 v[2:5], v170 offset:12288
	ds_read_b64 v[6:7], v173 offset:12352
	ds_read_b128 v[8:11], v170 offset:13824
	ds_read_b64 v[12:13], v173 offset:13888
	ds_read_b128 v[14:17], v170 offset:15360
	ds_read_b64 v[18:19], v173 offset:15424
	ds_read_b128 v[26:29], v170 offset:16896
	ds_read_b64 v[30:31], v173 offset:16960
	v_mfma_scale_f32_16x16x128_f8f6f4 v[144:147], v[46:51], v[20:25], v[144:147], v187, v187 op_sel_hi:[0,0,0] cbsz:2 blgp:2
	v_mfma_scale_f32_16x16x128_f8f6f4 v[136:139], v[194:199], v[20:25], v[136:139], v187, v187 op_sel_hi:[0,0,0] cbsz:2 blgp:2
	v_mfma_scale_f32_16x16x128_f8f6f4 v[128:131], v[200:205], v[20:25], v[128:131], v187, v187 op_sel_hi:[0,0,0] cbsz:2 blgp:2
	v_mfma_scale_f32_16x16x128_f8f6f4 v[120:123], v[206:211], v[20:25], v[120:123], v187, v187 op_sel_hi:[0,0,0] cbsz:2 blgp:2
	v_mfma_scale_f32_16x16x128_f8f6f4 v[116:119], v[46:51], v[32:37], v[116:119], v187, v187 op_sel_hi:[0,0,0] cbsz:2 blgp:2
	v_mfma_scale_f32_16x16x128_f8f6f4 v[108:111], v[194:199], v[32:37], v[108:111], v187, v187 op_sel_hi:[0,0,0] cbsz:2 blgp:2
	v_mfma_scale_f32_16x16x128_f8f6f4 v[104:107], v[200:205], v[32:37], v[104:107], v187, v187 op_sel_hi:[0,0,0] cbsz:2 blgp:2
	v_mfma_scale_f32_16x16x128_f8f6f4 v[96:99], v[206:211], v[32:37], v[96:99], v187, v187 op_sel_hi:[0,0,0] cbsz:2 blgp:2
	ds_read_b128 v[20:23], v1
	ds_read_b64 v[24:25], v172 offset:64
	ds_read_b128 v[32:35], v1 offset:1536
	ds_read_b64 v[36:37], v172 offset:1600
	s_cbranch_vccnz .Lpst3_other
	s_add_u32 s38, s72, 0x3000
	s_addc_u32 s39, s73, 0
	s_waitcnt vmcnt(0)
	s_barrier
	s_mov_b32 m0, s77
	s_nop 0
	global_load_lds_dwordx4 v228, s[38:39] offset:-3072
	global_load_lds_dwordx4 v228, s[38:39] offset:-2048
	global_load_lds_dwordx4 v228, s[38:39] offset:-1024
	global_load_lds_dwordx4 v228, s[38:39]
	global_load_lds_dwordx4 v228, s[38:39] offset:1024
	global_load_lds_dwordx4 v228, s[38:39] offset:2048
	s_branch .Lpst3_join

.LBB1_3:
	ds_read_b128 v[188:191], v1 offset:24576
	ds_read_b64 v[192:193], v172 offset:24640
	ds_read_b128 v[194:197], v1 offset:26112
	ds_read_b64 v[198:199], v172 offset:26176
	ds_read_b128 v[200:203], v170 offset:36864
	ds_read_b64 v[204:205], v173 offset:36928
	ds_read_b128 v[206:209], v170 offset:38400
	ds_read_b64 v[210:211], v173 offset:38464
	ds_read_b128 v[212:215], v170 offset:39936
	ds_read_b64 v[216:217], v173 offset:40000
	ds_read_b128 v[218:221], v170 offset:41472
	ds_read_b64 v[222:223], v173 offset:41536
	v_mfma_scale_f32_16x16x128_f8f6f4 v[164:167], v[2:7], v[20:25], v[164:167], v187, v187 op_sel_hi:[0,0,0] cbsz:2 blgp:2
	v_mfma_scale_f32_16x16x128_f8f6f4 v[160:163], v[8:13], v[20:25], v[160:163], v187, v187 op_sel_hi:[0,0,0] cbsz:2 blgp:2
	v_mfma_scale_f32_16x16x128_f8f6f4 v[156:159], v[14:19], v[20:25], v[156:159], v187, v187 op_sel_hi:[0,0,0] cbsz:2 blgp:2
	v_mfma_scale_f32_16x16x128_f8f6f4 v[152:155], v[26:31], v[20:25], v[152:155], v187, v187 op_sel_hi:[0,0,0] cbsz:2 blgp:2
	v_mfma_scale_f32_16x16x128_f8f6f4 v[148:151], v[2:7], v[32:37], v[148:151], v187, v187 op_sel_hi:[0,0,0] cbsz:2 blgp:2
	v_mfma_scale_f32_16x16x128_f8f6f4 v[140:143], v[8:13], v[32:37], v[140:143], v187, v187 op_sel_hi:[0,0,0] cbsz:2 blgp:2
	v_mfma_scale_f32_16x16x128_f8f6f4 v[132:135], v[14:19], v[32:37], v[132:135], v187, v187 op_sel_hi:[0,0,0] cbsz:2 blgp:2
	v_mfma_scale_f32_16x16x128_f8f6f4 v[124:127], v[26:31], v[32:37], v[124:127], v187, v187 op_sel_hi:[0,0,0] cbsz:2 blgp:2
	s_cbranch_vccz .Lst0_other
	s_add_u32 s38, s72, 0xffffa000
	s_addc_u32 s39, s73, -1
	s_waitcnt vmcnt(0)
	s_barrier
	s_mov_b32 m0, s76
	s_nop 0
	global_load_lds_dwordx4 v228, s[38:39] offset:-3072
	global_load_lds_dwordx4 v228, s[38:39] offset:-2048
	global_load_lds_dwordx4 v228, s[38:39] offset:-1024
	global_load_lds_dwordx4 v228, s[38:39]
	global_load_lds_dwordx4 v228, s[38:39] offset:1024
	global_load_lds_dwordx4 v228, s[38:39] offset:2048
	s_branch .Lst0_join

.Lst0_join:
	s_waitcnt lgkmcnt(0)
	v_mfma_scale_f32_16x16x128_f8f6f4 v[112:115], v[2:7], v[188:193], v[112:115], v187, v187 op_sel_hi:[0,0,0] cbsz:2 blgp:2
	v_mfma_scale_f32_16x16x128_f8f6f4 v[100:103], v[8:13], v[188:193], v[100:103], v187, v187 op_sel_hi:[0,0,0] cbsz:2 blgp:2
	v_mfma_scale_f32_16x16x128_f8f6f4 v[92:95], v[14:19], v[188:193], v[92:95], v187, v187 op_sel_hi:[0,0,0] cbsz:2 blgp:2
	v_mfma_scale_f32_16x16x128_f8f6f4 v[88:91], v[26:31], v[188:193], v[88:91], v187, v187 op_sel_hi:[0,0,0] cbsz:2 blgp:2
	v_mfma_scale_f32_16x16x128_f8f6f4 v[84:87], v[2:7], v[194:199], v[84:87], v187, v187 op_sel_hi:[0,0,0] cbsz:2 blgp:2
	v_mfma_scale_f32_16x16x128_f8f6f4 v[76:79], v[8:13], v[194:199], v[76:79], v187, v187 op_sel_hi:[0,0,0] cbsz:2 blgp:2
	v_mfma_scale_f32_16x16x128_f8f6f4 v[68:71], v[14:19], v[194:199], v[68:71], v187, v187 op_sel_hi:[0,0,0] cbsz:2 blgp:2
	v_mfma_scale_f32_16x16x128_f8f6f4 v[60:63], v[26:31], v[194:199], v[60:63], v187, v187 op_sel_hi:[0,0,0] cbsz:2 blgp:2
	ds_read_b128 v[2:5], v170 offset:61440
	ds_read_b64 v[6:7], v173 offset:61504
	ds_read_b128 v[8:11], v170 offset:62976
	ds_read_b64 v[12:13], v173 offset:63040
	ds_read_b128 v[14:17], v170 offset:64512
	ds_read_b64 v[18:19], v173 offset:64576
	ds_read_b128 v[26:29], v171 offset:53760
	ds_read_b64 v[30:31], v174 offset:53760
	v_mfma_scale_f32_16x16x128_f8f6f4 v[144:147], v[200:205], v[20:25], v[144:147], v187, v187 op_sel_hi:[0,0,0] cbsz:2 blgp:2
	v_mfma_scale_f32_16x16x128_f8f6f4 v[136:139], v[206:211], v[20:25], v[136:139], v187, v187 op_sel_hi:[0,0,0] cbsz:2 blgp:2
	v_mfma_scale_f32_16x16x128_f8f6f4 v[128:131], v[212:217], v[20:25], v[128:131], v187, v187 op_sel_hi:[0,0,0] cbsz:2 blgp:2
	v_mfma_scale_f32_16x16x128_f8f6f4 v[120:123], v[218:223], v[20:25], v[120:123], v187, v187 op_sel_hi:[0,0,0] cbsz:2 blgp:2
	v_mfma_scale_f32_16x16x128_f8f6f4 v[116:119], v[200:205], v[32:37], v[116:119], v187, v187 op_sel_hi:[0,0,0] cbsz:2 blgp:2
	v_mfma_scale_f32_16x16x128_f8f6f4 v[108:111], v[206:211], v[32:37], v[108:111], v187, v187 op_sel_hi:[0,0,0] cbsz:2 blgp:2
	v_mfma_scale_f32_16x16x128_f8f6f4 v[104:107], v[212:217], v[32:37], v[104:107], v187, v187 op_sel_hi:[0,0,0] cbsz:2 blgp:2
	v_mfma_scale_f32_16x16x128_f8f6f4 v[96:99], v[218:223], v[32:37], v[96:99], v187, v187 op_sel_hi:[0,0,0] cbsz:2 blgp:2
	ds_read_b128 v[20:23], v1 offset:49152
	ds_read_b64 v[24:25], v172 offset:49216
	ds_read_b128 v[32:35], v1 offset:50688
	ds_read_b64 v[36:37], v172 offset:50752
	s_cbranch_vccnz .Lst1_other
	s_add_u32 s38, s72, 0xffffd000
	s_addc_u32 s39, s73, -1
	s_waitcnt vmcnt(0)
	s_barrier
	s_mov_b32 m0, s76
	s_nop 0
	global_load_lds_dwordx4 v228, s[38:39] offset:-3072
	global_load_lds_dwordx4 v228, s[38:39] offset:-2048
	global_load_lds_dwordx4 v228, s[38:39] offset:-1024
	global_load_lds_dwordx4 v228, s[38:39]
	global_load_lds_dwordx4 v228, s[38:39] offset:1024
	global_load_lds_dwordx4 v228, s[38:39] offset:2048
	s_branch .Lst1_join

.Lst1_join:
	v_mfma_scale_f32_16x16x128_f8f6f4 v[80:83], v[200:205], v[188:193], v[80:83], v187, v187 op_sel_hi:[0,0,0] cbsz:2 blgp:2
	v_mfma_scale_f32_16x16x128_f8f6f4 v[72:75], v[206:211], v[188:193], v[72:75], v187, v187 op_sel_hi:[0,0,0] cbsz:2 blgp:2
	v_mfma_scale_f32_16x16x128_f8f6f4 v[64:67], v[212:217], v[188:193], v[64:67], v187, v187 op_sel_hi:[0,0,0] cbsz:2 blgp:2
	v_mfma_scale_f32_16x16x128_f8f6f4 v[56:59], v[218:223], v[188:193], v[56:59], v187, v187 op_sel_hi:[0,0,0] cbsz:2 blgp:2
	v_mfma_scale_f32_16x16x128_f8f6f4 v[52:55], v[200:205], v[194:199], v[52:55], v187, v187 op_sel_hi:[0,0,0] cbsz:2 blgp:2
	v_mfma_scale_f32_16x16x128_f8f6f4 v[224:227], v[206:211], v[194:199], v[48:51], v187, v187 op_sel_hi:[0,0,0] cbsz:2 blgp:2
	v_mfma_scale_f32_16x16x128_f8f6f4 v[212:215], v[212:217], v[194:199], v[44:47], v187, v187 op_sel_hi:[0,0,0] cbsz:2 blgp:2
	v_mfma_scale_f32_16x16x128_f8f6f4 v[216:219], v[218:223], v[194:199], v[40:43], v187, v187 op_sel_hi:[0,0,0] cbsz:2 blgp:2
	s_waitcnt lgkmcnt(0)
	s_nop 0
	ds_read_b128 v[40:43], v175
	ds_read_b64 v[44:45], v176
	ds_read_b128 v[188:191], v179
	ds_read_b64 v[192:193], v180
	ds_read_b128 v[46:49], v177
	ds_read_b64 v[50:51], v178
	ds_read_b128 v[194:197], v181
	ds_read_b64 v[198:199], v182
	ds_read_b128 v[200:203], v183
	ds_read_b64 v[204:205], v184
	ds_read_b128 v[206:209], v185
	ds_read_b64 v[210:211], v186
	v_mfma_scale_f32_16x16x128_f8f6f4 v[164:167], v[2:7], v[20:25], v[164:167], v187, v187 op_sel_hi:[0,0,0] cbsz:2 blgp:2
	v_mfma_scale_f32_16x16x128_f8f6f4 v[160:163], v[8:13], v[20:25], v[160:163], v187, v187 op_sel_hi:[0,0,0] cbsz:2 blgp:2
	v_mfma_scale_f32_16x16x128_f8f6f4 v[156:159], v[14:19], v[20:25], v[156:159], v187, v187 op_sel_hi:[0,0,0] cbsz:2 blgp:2
	v_mfma_scale_f32_16x16x128_f8f6f4 v[152:155], v[26:31], v[20:25], v[152:155], v187, v187 op_sel_hi:[0,0,0] cbsz:2 blgp:2
	v_mfma_scale_f32_16x16x128_f8f6f4 v[148:151], v[2:7], v[32:37], v[148:151], v187, v187 op_sel_hi:[0,0,0] cbsz:2 blgp:2
	v_mfma_scale_f32_16x16x128_f8f6f4 v[140:143], v[8:13], v[32:37], v[140:143], v187, v187 op_sel_hi:[0,0,0] cbsz:2 blgp:2
	v_mfma_scale_f32_16x16x128_f8f6f4 v[132:135], v[14:19], v[32:37], v[132:135], v187, v187 op_sel_hi:[0,0,0] cbsz:2 blgp:2
	v_mfma_scale_f32_16x16x128_f8f6f4 v[124:127], v[26:31], v[32:37], v[124:127], v187, v187 op_sel_hi:[0,0,0] cbsz:2 blgp:2
	s_cbranch_vccz .Lst2_other
	s_mov_b64 s[38:39], s[72:73]
	s_waitcnt vmcnt(0)
	s_barrier
	s_mov_b32 m0, s77
	s_nop 0
	global_load_lds_dwordx4 v228, s[38:39] offset:-3072
	global_load_lds_dwordx4 v228, s[38:39] offset:-2048
	global_load_lds_dwordx4 v228, s[38:39] offset:-1024
	global_load_lds_dwordx4 v228, s[38:39]
	global_load_lds_dwordx4 v228, s[38:39] offset:1024
	global_load_lds_dwordx4 v228, s[38:39] offset:2048
	s_branch .Lst2_join

.LBB1_5:
	ds_read_b128 v[188:191], v1 offset:24576
	ds_read_b64 v[192:193], v172 offset:24640
	ds_read_b128 v[194:197], v1 offset:26112
	ds_read_b64 v[198:199], v172 offset:26176
	ds_read_b128 v[200:203], v170 offset:36864
	ds_read_b64 v[204:205], v173 offset:36928
	ds_read_b128 v[206:209], v170 offset:38400
	ds_read_b64 v[210:211], v173 offset:38464
	ds_read_b128 v[212:215], v170 offset:39936
	ds_read_b64 v[216:217], v173 offset:40000
	ds_read_b128 v[218:221], v170 offset:41472
	ds_read_b64 v[222:223], v173 offset:41536
	v_mfma_scale_f32_16x16x128_f8f6f4 v[164:167], v[2:7], v[20:25], v[164:167], v187, v187 op_sel_hi:[0,0,0] cbsz:2 blgp:2
	v_mfma_scale_f32_16x16x128_f8f6f4 v[160:163], v[8:13], v[20:25], v[160:163], v187, v187 op_sel_hi:[0,0,0] cbsz:2 blgp:2
	v_mfma_scale_f32_16x16x128_f8f6f4 v[156:159], v[14:19], v[20:25], v[156:159], v187, v187 op_sel_hi:[0,0,0] cbsz:2 blgp:2
	v_mfma_scale_f32_16x16x128_f8f6f4 v[152:155], v[26:31], v[20:25], v[152:155], v187, v187 op_sel_hi:[0,0,0] cbsz:2 blgp:2
	v_mfma_scale_f32_16x16x128_f8f6f4 v[148:151], v[2:7], v[32:37], v[148:151], v187, v187 op_sel_hi:[0,0,0] cbsz:2 blgp:2
	v_mfma_scale_f32_16x16x128_f8f6f4 v[140:143], v[8:13], v[32:37], v[140:143], v187, v187 op_sel_hi:[0,0,0] cbsz:2 blgp:2
	v_mfma_scale_f32_16x16x128_f8f6f4 v[132:135], v[14:19], v[32:37], v[132:135], v187, v187 op_sel_hi:[0,0,0] cbsz:2 blgp:2
	v_mfma_scale_f32_16x16x128_f8f6f4 v[124:127], v[26:31], v[32:37], v[124:127], v187, v187 op_sel_hi:[0,0,0] cbsz:2 blgp:2
	s_cbranch_vccz .Ltail_nowait
	s_waitcnt vmcnt(0)
